# P2 SSD unit: second dt row requested with the first; conv weight/bias loads issued before the input-row loads
# speedup vs baseline: 1.0051x; 1.0051x over previous
; __device__ __forceinline__ float bf2f(bf16 b) { return __uint_as_float(((unsigned)b) << 16); }
; __device__ __forceinline__ float softplus_f(float x) { return x > 20.f ? x : log1pf(__expf(x)); }
; #define PROJ_AT(X, row, col) (XP_PROJ(X) + (size_t)((col) >> 8) * PANP + (size_t)(row) * 256 + ((col) & 255))
; __device__ __forceinline__ void p2_ssd(Ctx& X, int unit) {
;     ...
;     if (w < 4) { const int h = 8 * g + 4 * hh + w, l0 = 2 * lane;
;         const float dtb = XP_dt_bias(X)[h], A = -expf(XP_a_log(X)[h]);
;         const float d0 = softplus_f(bf2f(*PROJ_AT(X, t0 + l0, C_DT + h)) + dtb), d1 = softplus_f(bf2f(*PROJ_AT(X, t0 + l0 + 1, C_DT + h)) + dtb);
;         const float a0 = d0 * A, a1 = d1 * A, s = a0 + a1, incl = wave_incl_scan(s, lane);
;         dtS[w * 128 + l0] = d0; dtS[w * 128 + l0 + 1] = d1; acS[w * 128 + l0] = incl - a1; acS[w * 128 + l0 + 1] = incl;
;         if (lane == 63) XP_ADEC(X)[c * 16 + h] = expf(incl); }
;     ...
;         f32x4 wa[4], wb[4];
; #pragma unroll
;         for (int k = 0; k < 4; ++k) { wa[k] = *(const f32x4*)(XP_conv_w(X) + k * XBCW + cx); wb[k] = *(const f32x4*)(XP_conv_w(X) + k * XBCW + cx + 4); }
;         const f32x4 ba = *(const f32x4*)(XP_conv_b(X) + cx), bb = *(const f32x4*)(XP_conv_b(X) + cx + 4);
.LBB0_202:
	s_load_dwordx2 s[98:99], s[0:1], 0x20
	s_load_dwordx2 s[100:101], s[0:1], 0x28
	s_ashr_i32 s71, s70, 2
	s_bfe_u32 s72, s70, 0x10001
	s_and_b32 s73, s70, 1
	s_andn2_b64 vcc, exec, s[30:31]
	s_lshl_b32 s74, s71, 7
	s_cbranch_vccnz .LBB0_210
	s_lshl_b32 s36, s72, 3
	s_lshl_b32 s48, s73, 2
	s_or_b32 s36, s36, s48
	v_or_b32_e32 v4, s74, v145
	s_or_b32 s50, s36, s93
	s_load_dwordx4 s[52:55], s[0:1], 0x30
	v_ashrrev_i32_e32 v5, 31, v4
	s_lshl_b32 s36, s50, 2
	v_lshlrev_b64 v[2:3], 9, v[4:5]
	v_mov_b32_e32 v6, s36
	v_lshl_add_u64 v[2:3], s[34:35], 0, v[2:3]
	s_lshl_b32 s36, s50, 1
	v_lshl_add_u64 v[2:3], v[2:3], 0, s[36:37]
	global_load_ushort v252, v[2:3], off offset:512
	global_load_ushort v2, v[2:3], off
	s_waitcnt lgkmcnt(0)
	global_load_dword v3, v6, s[52:53]
	global_load_dword v5, v6, s[54:55]
	s_waitcnt vmcnt(2)
	v_lshlrev_b32_e32 v2, 16, v2
	s_waitcnt vmcnt(1)
	v_add_f32_e32 v2, v3, v2
	v_cmp_nlt_f32_e32 vcc, s61, v2
	s_and_saveexec_b64 s[48:49], vcc
	s_cbranch_execz .LBB0_205
	v_mul_f32_e32 v2, 0x3fb8aa3b, v2
	v_exp_f32_e32 v2, v2
	s_nop 0
	v_add_f32_e32 v8, 1.0, v2
	v_frexp_mant_f32_e32 v10, v8
	v_cvt_f64_f32_e32 v[6:7], v8
	v_frexp_exp_i32_f64_e32 v6, v[6:7]
	v_cmp_gt_f32_e32 vcc, s63, v10
	v_add_f32_e32 v9, -1.0, v8
	v_sub_f32_e32 v11, v9, v8
	v_subbrev_co_u32_e32 v14, vcc, 0, v6, vcc
	v_sub_u32_e32 v6, 0, v14
	v_sub_f32_e32 v9, v2, v9
	v_add_f32_e32 v11, 1.0, v11
	v_ldexp_f32 v7, v8, v6
	v_add_f32_e32 v9, v9, v11
	v_add_f32_e32 v8, -1.0, v7
	v_add_f32_e32 v10, 1.0, v7
	v_ldexp_f32 v6, v9, v6
	v_add_f32_e32 v9, 1.0, v8
	v_add_f32_e32 v11, -1.0, v10
	v_sub_f32_e32 v9, v7, v9
	v_sub_f32_e32 v7, v7, v11
	v_add_f32_e32 v9, v6, v9
	v_add_f32_e32 v6, v6, v7
	v_add_f32_e32 v15, v10, v6
	v_rcp_f32_e32 v17, v15
	v_sub_f32_e32 v7, v15, v10
	v_sub_f32_e32 v16, v6, v7
	v_add_f32_e32 v7, v8, v9
	v_mul_f32_e32 v19, v7, v17
	v_sub_f32_e32 v6, v7, v8
	v_mul_f32_e32 v8, v15, v19
	v_fma_f32 v10, v19, v15, -v8
	v_fmac_f32_e32 v10, v19, v16
	v_sub_f32_e32 v18, v9, v6
	v_add_f32_e32 v6, v8, v10
	v_sub_f32_e32 v9, v7, v6
	v_pk_add_f32 v[12:13], v[6:7], v[8:9] neg_lo:[0,1] neg_hi:[0,1]
	v_mov_b32_e32 v11, v6
	v_pk_add_f32 v[6:7], v[12:13], v[10:11] neg_lo:[0,1] neg_hi:[0,1]
	v_cmp_neq_f32_e32 vcc, s65, v2
	v_add_f32_e32 v7, v18, v7
	v_add_f32_e32 v6, v6, v7
	v_add_f32_e32 v7, v9, v6
	v_mul_f32_e32 v18, v17, v7
	v_mul_f32_e32 v8, v15, v18
	v_fma_f32 v10, v18, v15, -v8
	v_fmac_f32_e32 v10, v18, v16
	v_sub_f32_e32 v9, v9, v7
	v_add_f32_e32 v15, v6, v9
	v_add_f32_e32 v6, v8, v10
	v_sub_f32_e32 v9, v7, v6
	v_pk_add_f32 v[12:13], v[6:7], v[8:9] neg_lo:[0,1] neg_hi:[0,1]
	v_mov_b32_e32 v11, v6
	v_pk_add_f32 v[6:7], v[12:13], v[10:11] neg_lo:[0,1] neg_hi:[0,1]
	s_nop 0
	v_add_f32_e32 v7, v15, v7
	v_add_f32_e32 v6, v6, v7
	v_add_f32_e32 v7, v19, v18
	v_add_f32_e32 v6, v9, v6
	v_sub_f32_e32 v8, v7, v19
	v_mul_f32_e32 v6, v17, v6
	v_sub_f32_e32 v8, v18, v8
	v_add_f32_e32 v8, v8, v6
	v_add_f32_e32 v10, v7, v8
	v_mul_f32_e32 v11, v10, v10
	v_fmamk_f32 v6, v11, 0x3e9b6dac, v221
	v_fmaak_f32 v103, v11, v6, 0x3f2aaada
	v_cvt_f32_i32_e32 v6, v14
	v_sub_f32_e32 v7, v10, v7
	v_sub_f32_e32 v7, v8, v7
	v_ldexp_f32 v12, v7, 1
	v_mul_f32_e32 v7, v10, v11
	v_ldexp_f32 v9, v10, 1
	v_pk_mul_f32 v[10:11], v[6:7], v[102:103]
	s_nop 0
	v_fma_f32 v8, v6, s64, -v10
	v_fmac_f32_e32 v8, 0xb102e308, v6
	v_pk_add_f32 v[6:7], v[10:11], v[8:9]
	s_nop 0
	v_sub_f32_e32 v9, v7, v9
	v_sub_f32_e32 v9, v11, v9
	v_add_f32_e32 v13, v12, v9
	v_mov_b32_e32 v12, v10
	v_pk_add_f32 v[10:11], v[6:7], v[10:11] neg_lo:[0,1] neg_hi:[0,1]
	v_pk_add_f32 v[14:15], v[6:7], v[12:13]
	v_mov_b32_e32 v9, v6
	v_mov_b32_e32 v11, v15
	v_pk_add_f32 v[16:17], v[8:9], v[10:11] neg_lo:[0,1] neg_hi:[0,1]
	v_pk_add_f32 v[8:9], v[8:9], v[10:11]
	v_mov_b32_e32 v12, v13
	v_pk_add_f32 v[10:11], v[8:9], v[6:7] op_sel:[1,0] op_sel_hi:[0,1] neg_lo:[0,1] neg_hi:[0,1]
	v_pk_add_f32 v[18:19], v[14:15], v[10:11] op_sel_hi:[1,0] neg_lo:[0,1] neg_hi:[0,1]
	v_mov_b32_e32 v14, v15
	v_mov_b32_e32 v15, v9
	v_pk_mov_b32 v[10:11], v[6:7], v[10:11] op_sel:[1,0]
	v_mov_b32_e32 v13, v6
	v_pk_add_f32 v[10:11], v[14:15], v[10:11] neg_lo:[0,1] neg_hi:[0,1]
	v_mov_b32_e32 v18, v16
	v_pk_add_f32 v[6:7], v[12:13], v[10:11] neg_lo:[0,1] neg_hi:[0,1]
	v_mov_b32_e32 v17, v9
	v_pk_add_f32 v[10:11], v[18:19], v[6:7]
	s_nop 0
	v_pk_add_f32 v[12:13], v[10:11], v[10:11] op_sel:[0,1] op_sel_hi:[1,0]
	s_nop 0
	v_pk_add_f32 v[8:9], v[8:9], v[12:13] op_sel:[1,0] op_sel_hi:[0,1]
	v_mov_b32_e32 v11, v8
	v_pk_add_f32 v[14:15], v[10:11], v[16:17] neg_lo:[0,1] neg_hi:[0,1]
	v_mov_b32_e32 v7, v12
	v_sub_f32_e32 v9, v10, v14
	v_pk_add_f32 v[6:7], v[6:7], v[14:15] neg_lo:[0,1] neg_hi:[0,1]
	v_sub_f32_e32 v9, v16, v9
	v_add_f32_e32 v6, v6, v9
	v_add_f32_e32 v6, v6, v7
	v_add_f32_e32 v6, v8, v6
	v_cndmask_b32_e32 v6, v223, v6, vcc
	v_cmp_ngt_f32_e32 vcc, -1.0, v2
	s_nop 1
	v_cndmask_b32_e32 v6, v224, v6, vcc
	v_cmp_neq_f32_e32 vcc, -1.0, v2
	s_nop 1
	v_cndmask_b32_e32 v6, v225, v6, vcc
	v_cmp_lt_f32_e64 vcc, |v2|, s66
	s_nop 1
	v_cndmask_b32_e32 v2, v6, v2, vcc
; __device__ __forceinline__ float bf2f(bf16 b) { return __uint_as_float(((unsigned)b) << 16); }
; __device__ __forceinline__ float softplus_f(float x) { return x > 20.f ? x : log1pf(__expf(x)); }
; #define PROJ_AT(X, row, col) (XP_PROJ(X) + (size_t)((col) >> 8) * PANP + (size_t)(row) * 256 + ((col) & 255))
; __device__ __forceinline__ void p2_ssd(Ctx& X, int unit) {
;     ...
;         const float d0 = softplus_f(bf2f(*PROJ_AT(X, t0 + l0, C_DT + h)) + dtb), d1 = softplus_f(bf2f(*PROJ_AT(X, t0 + l0 + 1, C_DT + h)) + dtb);
;         const float a0 = d0 * A, a1 = d1 * A, s = a0 + a1, incl = wave_incl_scan(s, lane);
;         dtS[w * 128 + l0] = d0; dtS[w * 128 + l0 + 1] = d1; acS[w * 128 + l0] = incl - a1; acS[w * 128 + l0 + 1] = incl;
;         if (lane == 63) XP_ADEC(X)[c * 16 + h] = expf(incl); }
.LBB0_205:
	s_or_b64 exec, exec, s[48:49]
	s_waitcnt vmcnt(0)
	v_lshlrev_b32_e32 v4, 16, v252
	v_add_f32_e32 v3, v3, v4
	v_cmp_nlt_f32_e32 vcc, s61, v3
	s_and_saveexec_b64 s[48:49], vcc
	s_cbranch_execz .LBB0_207
	v_mul_f32_e32 v3, 0x3fb8aa3b, v3
	v_exp_f32_e32 v3, v3
	s_nop 0
	v_add_f32_e32 v4, 1.0, v3
	v_frexp_mant_f32_e32 v9, v4
	v_cvt_f64_f32_e32 v[6:7], v4
	v_add_f32_e32 v8, -1.0, v4
	v_frexp_exp_i32_f64_e32 v6, v[6:7]
	v_cmp_gt_f32_e32 vcc, s63, v9
	v_sub_f32_e32 v10, v8, v4
	v_sub_f32_e32 v8, v3, v8
	v_subbrev_co_u32_e32 v14, vcc, 0, v6, vcc
	v_add_f32_e32 v10, 1.0, v10
	v_sub_u32_e32 v6, 0, v14
	v_add_f32_e32 v8, v8, v10
	v_ldexp_f32 v4, v4, v6
	v_ldexp_f32 v6, v8, v6
	v_add_f32_e32 v8, -1.0, v4
	v_add_f32_e32 v7, 1.0, v8
	v_sub_f32_e32 v7, v4, v7
	v_add_f32_e32 v9, v6, v7
	v_add_f32_e32 v7, 1.0, v4
	v_add_f32_e32 v10, -1.0, v7
	v_sub_f32_e32 v4, v4, v10
	v_add_f32_e32 v4, v6, v4
	v_add_f32_e32 v15, v7, v4
	v_rcp_f32_e32 v16, v15
	v_sub_f32_e32 v6, v15, v7
	v_add_f32_e32 v7, v8, v9
	v_sub_f32_e32 v4, v4, v6
	v_mul_f32_e32 v18, v7, v16
	v_sub_f32_e32 v6, v7, v8
	v_mul_f32_e32 v8, v15, v18
	v_fma_f32 v10, v18, v15, -v8
	v_fmac_f32_e32 v10, v18, v4
	v_sub_f32_e32 v17, v9, v6
	v_add_f32_e32 v6, v8, v10
	v_sub_f32_e32 v9, v7, v6
	v_pk_add_f32 v[12:13], v[6:7], v[8:9] neg_lo:[0,1] neg_hi:[0,1]
	v_mov_b32_e32 v11, v6
	v_pk_add_f32 v[6:7], v[12:13], v[10:11] neg_lo:[0,1] neg_hi:[0,1]
	v_cmp_neq_f32_e32 vcc, s65, v3
	v_add_f32_e32 v7, v17, v7
	v_add_f32_e32 v6, v6, v7
	v_add_f32_e32 v7, v9, v6
	v_mul_f32_e32 v17, v16, v7
	v_mul_f32_e32 v8, v15, v17
	v_fma_f32 v10, v17, v15, -v8
	v_fmac_f32_e32 v10, v17, v4
	v_sub_f32_e32 v4, v9, v7
	v_add_f32_e32 v4, v6, v4
	v_add_f32_e32 v6, v8, v10
	v_sub_f32_e32 v9, v7, v6
	v_pk_add_f32 v[12:13], v[6:7], v[8:9] neg_lo:[0,1] neg_hi:[0,1]
	v_mov_b32_e32 v11, v6
	v_pk_add_f32 v[6:7], v[12:13], v[10:11] neg_lo:[0,1] neg_hi:[0,1]
	s_nop 0
	v_add_f32_e32 v4, v4, v7
	v_add_f32_e32 v4, v6, v4
	v_add_f32_e32 v7, v18, v17
	v_add_f32_e32 v4, v9, v4
	v_sub_f32_e32 v6, v7, v18
	v_mul_f32_e32 v4, v16, v4
	v_sub_f32_e32 v6, v17, v6
	v_add_f32_e32 v4, v6, v4
	v_add_f32_e32 v8, v7, v4
	v_mul_f32_e32 v10, v8, v8
	v_fmamk_f32 v6, v10, 0x3e9b6dac, v221
	v_fmaak_f32 v103, v10, v6, 0x3f2aaada
	v_cvt_f32_i32_e32 v6, v14
	v_sub_f32_e32 v7, v8, v7
	v_sub_f32_e32 v4, v4, v7
	v_mul_f32_e32 v7, v8, v10
	v_pk_mul_f32 v[10:11], v[6:7], v[102:103]
	v_ldexp_f32 v9, v8, 1
	v_fma_f32 v8, v6, s64, -v10
	v_fmac_f32_e32 v8, 0xb102e308, v6
	v_pk_add_f32 v[6:7], v[10:11], v[8:9]
	v_ldexp_f32 v4, v4, 1
	v_sub_f32_e32 v9, v7, v9
	v_sub_f32_e32 v9, v11, v9
	v_add_f32_e32 v13, v4, v9
	v_mov_b32_e32 v12, v10
	v_pk_add_f32 v[10:11], v[6:7], v[10:11] neg_lo:[0,1] neg_hi:[0,1]
	v_pk_add_f32 v[14:15], v[6:7], v[12:13]
	v_mov_b32_e32 v9, v6
	v_mov_b32_e32 v11, v15
	v_pk_add_f32 v[16:17], v[8:9], v[10:11] neg_lo:[0,1] neg_hi:[0,1]
	v_pk_add_f32 v[8:9], v[8:9], v[10:11]
	v_mov_b32_e32 v12, v13
	v_pk_add_f32 v[10:11], v[8:9], v[6:7] op_sel:[1,0] op_sel_hi:[0,1] neg_lo:[0,1] neg_hi:[0,1]
	v_pk_add_f32 v[18:19], v[14:15], v[10:11] op_sel_hi:[1,0] neg_lo:[0,1] neg_hi:[0,1]
	v_mov_b32_e32 v14, v15
	v_mov_b32_e32 v15, v9
	v_pk_mov_b32 v[10:11], v[6:7], v[10:11] op_sel:[1,0]
	v_mov_b32_e32 v13, v6
	v_pk_add_f32 v[10:11], v[14:15], v[10:11] neg_lo:[0,1] neg_hi:[0,1]
	v_mov_b32_e32 v18, v16
	v_pk_add_f32 v[6:7], v[12:13], v[10:11] neg_lo:[0,1] neg_hi:[0,1]
	v_mov_b32_e32 v17, v9
	v_pk_add_f32 v[10:11], v[18:19], v[6:7]
	s_nop 0
	v_pk_add_f32 v[12:13], v[10:11], v[10:11] op_sel:[0,1] op_sel_hi:[1,0]
	s_nop 0
	v_pk_add_f32 v[8:9], v[8:9], v[12:13] op_sel:[1,0] op_sel_hi:[0,1]
	v_mov_b32_e32 v11, v8
	v_pk_add_f32 v[14:15], v[10:11], v[16:17] neg_lo:[0,1] neg_hi:[0,1]
	v_mov_b32_e32 v7, v12
	v_sub_f32_e32 v4, v10, v14
	v_pk_add_f32 v[6:7], v[6:7], v[14:15] neg_lo:[0,1] neg_hi:[0,1]
	v_sub_f32_e32 v4, v16, v4
	v_add_f32_e32 v4, v6, v4
	v_add_f32_e32 v4, v4, v7
	v_add_f32_e32 v4, v8, v4
	v_cndmask_b32_e32 v4, v223, v4, vcc
	v_cmp_ngt_f32_e32 vcc, -1.0, v3
	s_nop 1
	v_cndmask_b32_e32 v4, v224, v4, vcc
	v_cmp_neq_f32_e32 vcc, -1.0, v3
	s_nop 1
	v_cndmask_b32_e32 v4, v225, v4, vcc
	v_cmp_lt_f32_e64 vcc, |v3|, s66
	s_nop 1
	v_cndmask_b32_e32 v3, v4, v3, vcc

; #define PROJ_AT(X, row, col) (XP_PROJ(X) + (size_t)((col) >> 8) * PANP + (size_t)(row) * 256 + ((col) & 255))
; __device__ __forceinline__ void p2_ssd(Ctx& X, int unit) {
;     ...
;         int cx; if (j < 32) cx = 512 * g + 256 * hh + 8 * j; else if (j < 48) cx = 1024 + 128 * g + 8 * (j - 32); else cx = 1280 + 128 * g + 64 * hh + 8 * (j - 48);
;         u32x4 rw[18];
;         const bf16* cbase = PROJ_AT(X, t0 + l0 - 3, C_X + cx);
; #pragma unroll
;         for (int r = 0; r < 18; ++r) { const int l = l0 - 3 + r, tt = t0 + l; rw[r] = (tt >= 0 && l < 128) ? __builtin_nontemporal_load((const u32x4*)(cbase + r * 256)) : (u32x4){0u, 0u, 0u, 0u}; }
;         f32x4 wa[4], wb[4];
; #pragma unroll
;         for (int k = 0; k < 4; ++k) { wa[k] = *(const f32x4*)(XP_conv_w(X) + k * XBCW + cx); wb[k] = *(const f32x4*)(XP_conv_w(X) + k * XBCW + cx + 4); }
;         const f32x4 ba = *(const f32x4*)(XP_conv_b(X) + cx), bb = *(const f32x4*)(XP_conv_b(X) + cx + 4);
.LBB0_217:
	s_andn2_saveexec_b64 s[50:51], s[50:51]
	s_lshl_b32 s36, s72, 9
	s_lshl_b32 s52, s73, 8
	s_or_b32 s36, s36, s52
	v_add_u32_e32 v104, s36, v149
	s_or_b64 exec, exec, s[50:51]
	v_ashrrev_i32_e32 v105, 31, v104
	v_lshlrev_b64 v[250:251], 2, v[104:105]
	s_waitcnt lgkmcnt(0)
	v_lshl_add_u64 v[8:9], s[98:99], 0, v[250:251]
	v_add_co_u32_e32 v14, vcc, 0x1000, v8
	global_load_dwordx4 v[10:13], v[8:9], off offset:16
	global_load_dwordx4 v[18:21], v[8:9], off
	v_addc_co_u32_e32 v15, vcc, 0, v9, vcc
	global_load_dwordx4 v[108:111], v[14:15], off offset:2048
	v_lshl_add_u64 v[14:15], v[8:9], 0, s[42:43]
	global_load_dwordx4 v[114:117], v[14:15], off offset:16
	v_add_co_u32_e32 v14, vcc, 0x3000, v8
	v_lshl_add_u64 v[250:251], s[100:101], 0, v[250:251]
	s_nop 0
	v_addc_co_u32_e32 v15, vcc, 0, v9, vcc
	global_load_dwordx4 v[14:17], v[14:15], off
	s_nop 0
	global_load_dwordx4 v[26:29], v[250:251], off
	global_load_dwordx4 v[22:25], v[250:251], off offset:16
	v_add_co_u32_e32 v250, vcc, 0x4000, v8
	s_nop 1
	v_addc_co_u32_e32 v251, vcc, 0, v9, vcc
	global_load_dwordx4 v[118:121], v[250:251], off offset:2048
	v_lshl_add_u64 v[252:253], v[8:9], 0, s[44:45]
	v_lshl_add_u64 v[250:251], v[8:9], 0, s[46:47]
	global_load_dwordx4 v[230:233], v[250:251], off offset:16
	s_nop 0
	global_load_dwordx4 v[244:247], v[252:253], off offset:16
	v_add_u32_e32 v2, 0x1400, v104
	v_ashrrev_i32_e32 v2, 8, v2
	v_ashrrev_i32_e32 v3, 31, v2
	v_add_u32_e32 v4, s74, v152
	v_lshlrev_b64 v[2:3], 22, v[2:3]
	v_ashrrev_i32_e32 v5, 31, v4
	v_lshl_add_u64 v[2:3], s[28:29], 0, v[2:3]
	v_lshlrev_b64 v[4:5], 9, v[4:5]
	v_lshl_add_u64 v[2:3], v[2:3], 0, v[4:5]
	v_lshlrev_b32_sdwa v98, v227, v104 dst_sel:DWORD dst_unused:UNUSED_PAD src0_sel:DWORD src1_sel:BYTE_0
	v_lshl_add_u64 v[6:7], v[2:3], 0, v[98:99]
	v_cmp_gt_i32_e32 vcc, s74, v153
	v_mov_b32_e32 v90, 0
	v_mov_b32_e32 v94, 0
	v_mov_b32_e32 v95, 0
	v_mov_b32_e32 v96, 0
	v_mov_b32_e32 v97, 0
	s_and_saveexec_b64 s[50:51], vcc
	s_cbranch_execz .LBB0_221
	global_load_dwordx4 v[94:97], v[6:7], off nt

; __device__ __forceinline__ unsigned pk_bf16(float lo, float hi) { unsigned r; asm("v_cvt_pk_bf16_f32 %0, %1, %2" : "=v"(r) : "v"(lo), "v"(hi)); return r; }
; __device__ __forceinline__ float bf_lo(unsigned u) { return __uint_as_float(u << 16); }
; __device__ __forceinline__ float bf_hi(unsigned u) { return __uint_as_float(u & 0xffff0000u); }
; __device__ __forceinline__ float silu_f(float x) { return x * __builtin_amdgcn_rcpf(1.0f + __expf(-x)); }
; __device__ __forceinline__ void p2_ssd(Ctx& X, int unit) {
;     ...
;         f32x4 wa[4], wb[4];
; #pragma unroll
;         for (int k = 0; k < 4; ++k) { wa[k] = *(const f32x4*)(XP_conv_w(X) + k * XBCW + cx); wb[k] = *(const f32x4*)(XP_conv_w(X) + k * XBCW + cx + 4); }
;         const f32x4 ba = *(const f32x4*)(XP_conv_b(X) + cx), bb = *(const f32x4*)(XP_conv_b(X) + cx + 4);
; #pragma unroll
;         for (int r = 0; r < 15; ++r) { const int l = l0 + r;
;             if (l < 128) { float o[8] = {ba.x, ba.y, ba.z, ba.w, bb.x, bb.y, bb.z, bb.w};
; #pragma unroll
;                 for (int k = 0; k < 4; ++k) { const u32x4 v = rw[r + k];
;                     o[0] += wa[k].x * bf_lo(v.x); o[1] += wa[k].y * bf_hi(v.x); o[2] += wa[k].z * bf_lo(v.y); o[3] += wa[k].w * bf_hi(v.y);
;                     o[4] += wb[k].x * bf_lo(v.z); o[5] += wb[k].y * bf_hi(v.z); o[6] += wb[k].z * bf_lo(v.w); o[7] += wb[k].w * bf_hi(v.w); }
; #pragma unroll
;                 for (int i = 0; i < 8; ++i) o[i] = silu_f(o[i]);
;                 u32x4 ov; ov.x = pk_bf16(o[0], o[1]); ov.y = pk_bf16(o[2], o[3]); ov.z = pk_bf16(o[4], o[5]); ov.w = pk_bf16(o[6], o[7]);
.LBB0_255:
	s_or_b64 exec, exec, s[50:51]
	s_waitcnt vmcnt(0)
	v_lshlrev_b32_e32 v127, 16, v94
	v_lshlrev_b32_e32 v126, 16, v90
	v_and_b32_e32 v135, 0xffff0000, v95
	v_mov_b32_e32 v6, v244
	v_mov_b32_e32 v7, v245
	v_mov_b32_e32 v8, v246
	v_mov_b32_e32 v9, v247
	v_and_b32_e32 v134, 0xffff0000, v91
	v_lshlrev_b32_e32 v141, 16, v97
	v_and_b32_e32 v143, 0xffff0000, v97
	v_and_b32_e32 v130, 0xffff0000, v90
	v_lshlrev_b32_e32 v132, 16, v91
	v_lshlrev_b32_e32 v133, 16, v95
	v_lshlrev_b32_e32 v137, 16, v96
	v_and_b32_e32 v139, 0xffff0000, v96
	v_and_b32_e32 v138, 0xffff0000, v92
	v_lshlrev_b32_e32 v140, 16, v93
	v_and_b32_e32 v142, 0xffff0000, v93
	v_and_b32_e32 v131, 0xffff0000, v94
	v_lshlrev_b32_e32 v136, 16, v92
	v_lshlrev_b32_e32 v113, 16, v86
	v_lshlrev_b32_e32 v112, 16, v82
	s_cmp_eq_u32 s73, 0
	s_cselect_b64 s[50:51], -1, 0
	s_mov_b64 s[52:53], 0
	s_waitcnt vmcnt(9)
	v_mov_b32_e32 v93, v10
	s_waitcnt vmcnt(8)
	v_mov_b32_e32 v107, v18
	v_mov_b32_e32 v97, v20
	v_mov_b32_e32 v91, v12
	s_waitcnt vmcnt(7)
	v_mov_b32_e32 v106, v108
	v_mov_b32_e32 v20, v111
	v_mov_b32_e32 v18, v109
	v_mov_b32_e32 v96, v110
	s_waitcnt vmcnt(6)
	v_mov_b32_e32 v10, v115
	v_mov_b32_e32 v90, v116
	v_mov_b32_e32 v12, v117
	v_pk_mul_f32 v[108:109], v[106:107], v[126:127]
	v_pk_mul_f32 v[116:117], v[20:21], v[134:135]
	v_mov_b32_e32 v92, v114
	v_pk_mul_f32 v[114:115], v[96:97], v[132:133]
	v_pk_mul_f32 v[124:125], v[10:11], v[138:139]
	s_waitcnt vmcnt(5)
	v_mov_b32_e32 v95, v14
	s_waitcnt vmcnt(4)
	v_add_f32_e32 v14, v109, v26
	v_add_f32_e32 v109, v117, v29
	s_waitcnt vmcnt(2)
	v_mov_b32_e32 v94, v118
	v_pk_mul_f32 v[110:111], v[18:19], v[130:131]
	v_pk_mul_f32 v[122:123], v[92:93], v[136:137]
	v_pk_mul_f32 v[234:235], v[12:13], v[142:143]
	v_add_f32_e32 v103, v115, v28
	v_add_f32_e32 v115, v125, v23
	v_add_f32_e32 v14, v108, v14
	v_add_f32_e32 v125, v116, v109
	v_pk_mul_f32 v[108:109], v[94:95], v[112:113]
	v_add_f32_e32 v98, v111, v27
	v_add_f32_e32 v111, v123, v22
	v_add_f32_e32 v123, v235, v25
	v_add_f32_e32 v14, v109, v14
	v_add_f32_e32 v103, v114, v103
	v_add_f32_e32 v124, v124, v115
	v_add_f32_e32 v229, v234, v123
	v_add_f32_e32 v234, v108, v14
	v_and_b32_e32 v115, 0xffff0000, v86
	v_and_b32_e32 v114, 0xffff0000, v82
	v_mov_b32_e32 v14, v119
	v_pk_mul_f32 v[128:129], v[90:91], v[140:141]
	v_add_f32_e32 v98, v110, v98
	v_pk_mul_f32 v[108:109], v[14:15], v[114:115]
	v_add_f32_e32 v117, v129, v24
	v_add_f32_e32 v82, v109, v98
	v_add_f32_e32 v128, v128, v117
	v_add_f32_e32 v98, v108, v82
	v_lshlrev_b32_e32 v116, 16, v83
	v_lshlrev_b32_e32 v117, 16, v87
	v_mov_b32_e32 v108, v120
	v_mov_b32_e32 v109, v16
	v_add_f32_e32 v122, v122, v111
	v_pk_mul_f32 v[110:111], v[108:109], v[116:117]
	v_and_b32_e32 v119, 0xffff0000, v87
	v_add_f32_e32 v16, v111, v103
	v_add_f32_e32 v103, v110, v16
	v_and_b32_e32 v118, 0xffff0000, v83
	v_mov_b32_e32 v16, v121
	v_pk_mul_f32 v[82:83], v[16:17], v[118:119]
	v_lshlrev_b32_e32 v121, 16, v88
	v_add_f32_e32 v83, v83, v125
	v_lshlrev_b32_e32 v120, 16, v84
	s_waitcnt vmcnt(1)
	v_mov_b32_e32 v86, v230
	s_waitcnt vmcnt(0)
	v_mov_b32_e32 v87, v6
	v_add_f32_e32 v235, v82, v83
	v_pk_mul_f32 v[82:83], v[86:87], v[120:121]
	v_and_b32_e32 v123, 0xffff0000, v88
	v_add_f32_e32 v6, v83, v122
	v_add_f32_e32 v230, v82, v6
	v_and_b32_e32 v122, 0xffff0000, v84
	v_mov_b32_e32 v6, v231
	v_pk_mul_f32 v[82:83], v[6:7], v[122:123]
	v_lshlrev_b32_e32 v125, 16, v89
	v_add_f32_e32 v83, v83, v124
	v_lshlrev_b32_e32 v124, 16, v85
	v_mov_b32_e32 v110, v232
	v_mov_b32_e32 v111, v8
	v_add_f32_e32 v84, v82, v83
	v_pk_mul_f32 v[82:83], v[110:111], v[124:125]
	v_and_b32_e32 v129, 0xffff0000, v89
	v_add_f32_e32 v8, v83, v128
	v_add_f32_e32 v232, v82, v8
	v_mul_f32_e32 v82, 0xbfb8aa3b, v234
	v_and_b32_e32 v128, 0xffff0000, v85
	v_exp_f32_e32 v85, v82
	v_mov_b32_e32 v8, v233
	v_pk_mul_f32 v[82:83], v[8:9], v[128:129]
	v_mul_f32_e32 v88, 0xbfb8aa3b, v103
	v_add_f32_e32 v83, v83, v229
	v_add_f32_e32 v82, v82, v83
	v_add_f32_e32 v83, 1.0, v85
	v_mul_f32_e32 v85, 0xbfb8aa3b, v98
	v_exp_f32_e32 v88, v88
	v_exp_f32_e32 v85, v85
	v_rcp_f32_e32 v83, v83
	v_add_f32_e32 v88, 1.0, v88
	v_add_f32_e32 v85, 1.0, v85
	v_rcp_f32_e32 v229, v88
	v_mul_f32_e32 v88, 0xbfb8aa3b, v235
	v_rcp_f32_e32 v85, v85
	v_exp_f32_e32 v231, v88
	v_mul_f32_e32 v88, v234, v83
	v_mul_f32_e32 v89, v98, v85
	v_mul_f32_e32 v98, v103, v229
	v_add_f32_e32 v83, 1.0, v231
	v_mul_f32_e32 v85, 0xbfb8aa3b, v230
	v_mul_f32_e32 v103, 0xbfb8aa3b, v84
	v_rcp_f32_e32 v83, v83
	v_exp_f32_e32 v85, v85
	v_exp_f32_e32 v229, v103
	v_mul_f32_e32 v231, 0xbfb8aa3b, v82
	v_mul_f32_e32 v103, v235, v83
	v_add_f32_e32 v83, 1.0, v85
	v_add_f32_e32 v85, 1.0, v229
	v_mul_f32_e32 v229, 0xbfb8aa3b, v232
	v_exp_f32_e32 v229, v229
	v_exp_f32_e32 v231, v231
	v_rcp_f32_e32 v83, v83
	v_rcp_f32_e32 v85, v85
	v_add_f32_e32 v229, 1.0, v229
	v_rcp_f32_e32 v233, v229
	v_add_f32_e32 v229, 1.0, v231
	v_rcp_f32_e32 v234, v229
	v_mul_f32_e32 v231, v230, v83
	v_mul_f32_e32 v229, v84, v85
	v_mul_f32_e32 v230, v232, v233
	v_mul_f32_e32 v232, v82, v234
	v_cvt_pk_bf16_f32 v82, v88, v89
	v_cvt_pk_bf16_f32 v83, v98, v103
	v_cvt_pk_bf16_f32 v84, v231, v229
	v_cvt_pk_bf16_f32 v85, v230, v232
	s_and_saveexec_b64 s[54:55], s[18:19]
	s_xor_b64 s[54:55], exec, s[54:55]
	s_cbranch_execnz .LBB0_287
	s_andn2_saveexec_b64 s[54:55], s[54:55]
	s_cbranch_execnz .LBB0_290
